# attention phase: per-XCD work queue split into attention-unit queue and weight-copy-chunk queue; 3 of every 8 workgroups pull copy chunks first, others attention first, with stealing from the other qu
# baseline (speedup 1.0000x reference)
.LBB6_892:
	s_lshr_b32 s0, s96, 3
	s_and_b32 s0, s0, 7
	s_cmp_lt_u32 s0, 3
	s_cselect_b32 s94, 0x80, 0
	s_and_saveexec_b64 s[2:3], s[68:69]
	s_cbranch_execz .Lpop1_b
	s_mov_b64 s[6:7], exec
	v_mbcnt_lo_u32_b32 v2, s6, 0
	v_mbcnt_hi_u32_b32 v2, s7, v2
	v_cmp_eq_u32_e32 vcc, 0, v2
	s_waitcnt lgkmcnt(0)
	s_and_saveexec_b64 s[4:5], vcc
	s_cbranch_execz .Lpop1_a
	s_bcnt1_i32_b64 s0, s[6:7]
	s_waitcnt vmcnt(0)
	v_mov_b32_e32 v4, s0
	v_mov_b32_e32 v5, s94
	global_atomic_add v4, v5, v4, s[8:9] sc0

.Lpop1_b:
	s_or_b64 exec, exec, s[2:3]
	v_readlane_b32 s0, v254, 30
	s_waitcnt lgkmcnt(0)
	s_barrier
	v_mov_b32_e32 v2, s0
	ds_read_b32 v2, v2
	s_waitcnt lgkmcnt(0)
	s_barrier
	v_readfirstlane_b32 s0, v2
	s_cmp_gt_i32 s0, 63
	s_cbranch_scc0 .Lrole_have
	s_xor_b32 s94, s94, 0x80
	s_and_saveexec_b64 s[2:3], s[68:69]
	s_cbranch_execz .Lpop2_b
	s_mov_b64 s[6:7], exec
	v_mbcnt_lo_u32_b32 v2, s6, 0
	v_mbcnt_hi_u32_b32 v2, s7, v2
	v_cmp_eq_u32_e32 vcc, 0, v2
	s_waitcnt lgkmcnt(0)
	s_and_saveexec_b64 s[4:5], vcc
	s_cbranch_execz .Lpop2_a
	s_bcnt1_i32_b64 s0, s[6:7]
	s_waitcnt vmcnt(0)
	v_mov_b32_e32 v4, s0
	v_mov_b32_e32 v5, s94
	global_atomic_add v4, v5, v4, s[8:9] sc0

.Lpop2_b:
	s_or_b64 exec, exec, s[2:3]
	v_readlane_b32 s0, v254, 30
	s_waitcnt lgkmcnt(0)
	s_barrier
	v_mov_b32_e32 v2, s0
	ds_read_b32 v2, v2
	s_waitcnt lgkmcnt(0)
	s_barrier
	v_readfirstlane_b32 s0, v2
	s_mov_b64 s[2:3], -1
	s_cmp_gt_i32 s0, 63
	s_cbranch_scc1 .LBB6_891
.Lrole_have:
	s_mov_b64 s[2:3], -1
	s_cmp_gt_i32 s0, 47
	s_cbranch_scc0 .LBB6_899
	s_sub_i32 s1, s0, 48
	s_lshr_b32 s92, s1, 1
	s_mov_b64 s[2:3], 0

.LBB6_901:
	s_lshl_b32 s84, s0, 3
	s_or_b32 s1, s84, s59
	s_mul_hi_i32 s3, s63, s1
	s_mul_i32 s2, s63, s1
	s_lshr_b64 s[2:3], s[2:3], 9
	s_add_i32 s1, s1, 1
	s_and_b32 s90, s2, 0xffffffe0
	s_mul_hi_i32 s3, s63, s1
	s_mul_i32 s2, s63, s1
	s_lshr_b64 s[2:3], s[2:3], 9
	s_and_b32 s91, s2, 0xffffffe0
	s_cmp_eq_u32 s94, 0
	s_cselect_b32 s90, 0, s90
	s_cselect_b32 s91, 0, s91
	s_cselect_b32 s93, s93, 7
	s_bitcmp0_b32 s0, 0
	s_cselect_b64 s[22:23], -1, 0
	s_and_b64 vcc, exec, s[22:23]
	s_cbranch_vccnz .LBB6_1210
	v_readlane_b32 s6, v254, 13
	v_readlane_b32 s7, v254, 14
	s_waitcnt vmcnt(0)
	v_mov_b32_e32 v167, v0
	s_max_i32 s64, s90, 0
	v_readfirstlane_b32 s0, v167
	s_ashr_i32 s95, s0, 6
	v_readlane_b32 s0, v254, 60
	s_lshl_b32 s81, s95, 14
	v_readlane_b32 s1, v254, 61
	v_and_b32_e32 v166, 63, v167
	s_add_i32 s94, s81, 0
	s_mov_b64 s[2:3], -1
	s_and_b64 vcc, exec, s[0:1]
	s_cbranch_vccz .LBB6_915
	s_min_i32 s30, s91, 0xdc00
	s_cmp_le_i32 s30, s64
	s_cbranch_scc1 .LBB6_908
	s_sub_i32 s0, s30, s64
	s_mov_b32 s2, 18
	s_cmp_lt_i32 s0, 32
	s_cbranch_scc1 .LBB6_908
	s_add_i32 s31, s95, s64
	s_cmp_ge_i32 s31, s30
	s_cbranch_scc1 .LBB6_908
	s_ashr_i32 s3, s2, 31
	s_lshl_b64 s[0:1], s[2:3], 3
	s_add_u32 s0, s76, s0
	s_addc_u32 s1, s77, s1
	s_load_dwordx2 s[0:1], s[0:1], 0x0
	v_lshrrev_b32_e32 v4, 3, v166
	v_lshlrev_b32_e32 v2, 2, v166
	v_mul_u32_u24_e32 v5, 0x2c00, v4
	v_and_b32_e32 v6, 28, v2
	s_waitcnt lgkmcnt(0)
	s_add_u32 s34, s0, 0x10800000
	v_or_b32_e32 v2, v5, v6
	v_lshl_add_u32 v5, v6, 2, s94
	v_lshlrev_b32_e32 v6, 5, v166
	s_addc_u32 s35, s1, 0
	v_lshrrev_b32_e32 v135, 1, v166
	v_and_b32_e32 v132, 32, v6
	s_add_u32 s36, s6, 0x85280000
	v_mul_u32_u24_e32 v4, 0x84, v4
	v_mul_u32_u24_e32 v6, 0x84, v132
	v_lshlrev_b32_e32 v7, 2, v135
	v_and_b32_e32 v134, 31, v167
	s_addc_u32 s37, s7, 0
	v_lshlrev_b32_e32 v2, 2, v2
	v_add3_u32 v136, s94, v6, v7
	v_mov_b32_e32 v133, v3
	v_add_u32_e32 v137, v5, v4

.LBB6_1210:
	s_cmp_eq_u32 s93, 7
	s_cbranch_scc1 .LBB6_1306
	s_and_b32 s0, s84, 8
	s_or_b32 s0, s0, s59
	s_sub_i32 s37, 7, s92
	s_lshr_b32 s36, s0, 2
	s_mov_b64 s[6:7], -1
	s_mov_b64 s[2:3], 0
	s_cmp_lt_i32 s93, 1
	s_mov_b64 s[4:5], 0
	s_cbranch_scc1 .LBB6_1224
	s_cmp_gt_i32 s93, 1
	s_cbranch_scc0 .LBB6_1252
	s_cmp_eq_u32 s93, 2
	s_mov_b64 s[4:5], -1
	s_cbranch_scc0 .LBB6_1251
	s_lshl_b32 s1, s37, 8
	s_lshl_b32 s6, s36, 11
	v_readlane_b32 s4, v254, 13
	s_add_i32 s0, s1, 0x100
	s_add_i32 s26, s1, s6
	v_readlane_b32 s5, v254, 14
	s_lshr_b32 s0, s0, 6
	s_mul_i32 s7, s26, 0x600
	s_mul_hi_u32 s6, s26, 0x600
	s_add_u32 s7, s4, s7
	s_addc_u32 s6, s5, s6
	s_add_u32 s7, s7, s71
	s_addc_u32 s6, s6, 0
	s_add_u32 s12, s7, 0x7200000
	s_addc_u32 s13, s6, 0
	s_mul_i32 s6, s36, 0x300000
	s_add_u32 s6, s4, s6
	s_addc_u32 s7, s5, 0
	s_add_u32 s6, s6, s71
	s_addc_u32 s7, s7, 0
	s_add_u32 s6, s6, 0x7e00000
	s_addc_u32 s7, s7, 0
	s_add_u32 s24, s4, s75
	s_addc_u32 s25, s5, 0
	s_lshl_b32 s27, s36, 12
	s_add_u32 s24, s24, s27
	v_mov_b32_e32 v183, v0
	s_addc_u32 s25, s25, 0
	s_waitcnt vmcnt(0)
	v_mov_b32_e32 v34, v0
	s_add_u32 s24, s24, 0xf300000
	s_addc_u32 s25, s25, 0
	v_readfirstlane_b32 s27, v34
	s_ashr_i32 s27, s27, 1
	s_movk_i32 s28, 0xffe0
	v_mov_b32_e32 v2, s27
	v_bfi_b32 v2, s28, v2, v34
	v_mov_b64_e32 v[4:5], s[12:13]
	v_bfe_u32 v35, v34, 5, 1
	v_mad_i64_i32 v[4:5], s[12:13], v2, s70, v[4:5]
	v_lshlrev_b32_e32 v2, 4, v35
	s_mov_b32 s12, 0x2aaaaaab
	v_lshl_add_u64 v[24:25], v[4:5], 0, v[2:3]
	v_mul_hi_i32 v4, v34, s12
	v_lshrrev_b32_e32 v5, 31, v4
	v_ashrrev_i32_e32 v4, 2, v4
	v_add_u32_e32 v189, v4, v5
	v_mul_lo_u32 v4, v189, 24
	v_sub_u32_e32 v36, v34, v4
	v_add_u32_e32 v4, 0x200, v34
	v_mul_hi_i32 v5, v4, s12
	v_lshrrev_b32_e32 v6, 31, v5
	v_ashrrev_i32_e32 v5, 2, v5
	v_add_u32_e32 v190, v5, v6
	v_mul_lo_u32 v5, v190, 24
	v_sub_u32_e32 v37, v4, v5
	v_add_u32_e32 v4, 0x400, v34
	v_mul_hi_i32 v5, v4, s12
	v_lshrrev_b32_e32 v6, 31, v5
	v_ashrrev_i32_e32 v5, 2, v5
	v_add_u32_e32 v192, v5, v6
	v_mul_lo_u32 v5, v192, 24
	v_sub_u32_e32 v38, v4, v5
	v_lshlrev_b32_e32 v14, 3, v38
	v_ashrrev_i32_e32 v15, 31, v14
	v_lshlrev_b32_e32 v6, 3, v36
	v_lshlrev_b32_e32 v8, 3, v37
	v_lshlrev_b64 v[32:33], 1, v[14:15]
	v_lshlrev_b32_e32 v14, 4, v34
	v_ashrrev_i32_e32 v39, 3, v34
	v_mov_b64_e32 v[26:27], s[6:7]
	v_ashrrev_i32_e32 v7, 31, v6
	v_ashrrev_i32_e32 v9, 31, v8
	v_and_b32_e32 v168, 0x70, v14
	v_mov_b32_e32 v169, v3
	v_mad_i64_i32 v[4:5], s[12:13], v189, s70, v[26:27]
	v_lshlrev_b64 v[28:29], 1, v[6:7]
	v_mad_i64_i32 v[6:7], s[12:13], v190, s70, v[26:27]
	v_lshlrev_b64 v[30:31], 1, v[8:9]
	v_mad_i64_i32 v[12:13], s[12:13], v192, s70, v[26:27]
	v_lshl_add_u64 v[170:171], s[24:25], 0, v[168:169]
	v_add_u32_e32 v40, 64, v39
	v_lshl_add_u64 v[4:5], v[4:5], 0, v[28:29]
	v_lshl_add_u64 v[8:9], v[6:7], 0, v[30:31]
	v_lshl_add_u64 v[12:13], v[12:13], 0, v[32:33]
	v_mad_i64_i32 v[16:17], s[12:13], v39, s55, v[170:171]
	v_mad_i64_i32 v[20:21], s[12:13], v40, s55, v[170:171]
	global_load_dwordx4 v[4:7], v[4:5], off
	s_nop 0
	global_load_dwordx4 v[8:11], v[8:9], off
	s_nop 0
	global_load_dwordx4 v[12:15], v[12:13], off
	s_nop 0
	global_load_dwordx4 v[16:19], v[16:17], off
	s_nop 0
	global_load_dwordx4 v[20:23], v[20:21], off
	s_nop 0
	global_load_dwordx4 v[144:147], v[24:25], off
	global_load_dwordx4 v[140:143], v[24:25], off offset:32
	global_load_dwordx4 v[136:139], v[24:25], off offset:64
	global_load_dwordx4 v[132:135], v[24:25], off offset:96
	global_load_dwordx4 v[128:131], v[24:25], off offset:128
	global_load_dwordx4 v[124:127], v[24:25], off offset:160
	global_load_dwordx4 v[120:123], v[24:25], off offset:192
	global_load_dwordx4 v[116:119], v[24:25], off offset:224
	global_load_dwordx4 v[112:115], v[24:25], off offset:256
	global_load_dwordx4 v[108:111], v[24:25], off offset:288
	global_load_dwordx4 v[104:107], v[24:25], off offset:320
	global_load_dwordx4 v[100:103], v[24:25], off offset:352
	v_add_u32_e32 v24, 64, v189
	v_mad_i64_i32 v[24:25], s[12:13], v24, s70, v[26:27]
	v_lshl_add_u64 v[24:25], v[24:25], 0, v[28:29]
	global_load_dwordx4 v[148:151], v[24:25], off
	v_add_u32_e32 v24, 64, v190
	v_mad_i64_i32 v[24:25], s[12:13], v24, s70, v[26:27]
	v_add_u32_e32 v41, 64, v192
	v_lshl_add_u64 v[24:25], v[24:25], 0, v[30:31]
	v_mad_i64_i32 v[26:27], s[12:13], v41, s70, v[26:27]
	v_lshl_add_u64 v[26:27], v[26:27], 0, v[32:33]
	global_load_dwordx4 v[152:155], v[24:25], off
	global_load_dwordx4 v[156:159], v[26:27], off
	v_mov_b64_e32 v[24:25], s[24:25]
	v_mad_i64_i32 v[26:27], s[12:13], v39, s55, v[24:25]
	v_lshl_add_u64 v[26:27], v[26:27], 0, v[168:169]
	v_mad_i64_i32 v[24:25], s[12:13], v40, s55, v[24:25]
	v_lshl_add_u64 v[24:25], v[24:25], 0, v[168:169]
	global_load_dwordx4 v[160:163], v[26:27], off offset:128
	global_load_dwordx4 v[164:167], v[24:25], off offset:128
	s_and_b32 s25, s27, 0xffffffe0
	s_add_i32 s12, s25, s1
	v_lshlrev_b32_e32 v24, 1, v34
	v_lshrrev_b32_e32 v25, 1, v34
	s_movk_i32 s1, 0x190
	v_and_b32_e32 v24, 8, v24
	v_and_b32_e32 v25, 4, v25
	v_and_b32_e32 v26, 19, v34
	v_mul_lo_u32 v194, v189, s1
	v_lshlrev_b32_e32 v195, 4, v36
	v_or3_b32 v24, v24, v26, v25
	v_add3_u32 v25, 0, v194, v195
	v_mul_lo_u32 v196, v190, s1
	v_lshlrev_b32_e32 v197, 4, v37
	v_mul_lo_u32 v198, v192, s1
	v_lshlrev_b32_e32 v199, 4, v38
	v_mul_lo_u32 v201, v39, s41
	v_and_b32_e32 v191, 31, v34
	v_mul_i32_i24_e32 v193, -8, v35
	s_lshl_b32 s1, s92, 8
	v_mad_i64_i32 v[172:173], s[28:29], v39, s55, 0
	v_mad_i64_i32 v[174:175], s[28:29], v40, s55, 0
	v_mul_u32_u24_e32 v200, 0x190, v24
	v_lshl_add_u64 v[176:177], s[6:7], 0, v[28:29]
	v_lshl_add_u64 v[178:179], s[6:7], 0, v[30:31]
	v_lshl_add_u64 v[184:185], s[6:7], 0, v[32:33]
	s_mov_b32 s24, 1
	s_or_b32 s13, s12, 31
	v_mul_u32_u24_e32 v169, 0x90, v191
	v_mov_b32_e32 v187, 0
	v_mov_b32_e32 v188, 0xf149f2ca
	s_movk_i32 s84, 0x80
	s_waitcnt vmcnt(21)
	ds_write_b128 v25, v[4:7]
	v_add3_u32 v4, 0, v196, v197
	s_waitcnt vmcnt(20)
	ds_write_b128 v4, v[8:11]
	v_add3_u32 v4, 0, v198, v199
	s_waitcnt vmcnt(19)
	ds_write_b128 v4, v[12:15]
	v_add3_u32 v4, 0, v168, v201
	s_waitcnt vmcnt(18)
	ds_write_b128 v4, v[16:19] offset:25600
	s_waitcnt vmcnt(17)
	ds_write_b128 v4, v[20:23] offset:34816
	v_add3_u32 v4, v193, s25, v191
	v_subrev_u32_e32 v4, s1, v4
	v_mov_b32_e32 v18, v3
	v_mov_b32_e32 v19, v3
	v_add_u32_e32 v202, 0x6e9, v4
	v_mov_b32_e32 v4, v3
	v_mov_b32_e32 v5, v3
	v_mov_b32_e32 v6, v3
	v_mov_b32_e32 v7, v3
	v_mov_b32_e32 v8, v3
	v_mov_b32_e32 v9, v3
	v_mov_b32_e32 v10, v3
	v_mov_b32_e32 v11, v3
	v_mov_b32_e32 v12, v3
	v_mov_b32_e32 v13, v3
	v_mov_b32_e32 v14, v3
	v_mov_b32_e32 v15, v3
	v_mov_b32_e32 v16, v3
	v_mov_b32_e32 v17, v3
	v_mov_b64_e32 v[34:35], v[18:19]
	v_mov_b64_e32 v[50:51], v[18:19]
	v_mov_b64_e32 v[66:67], v[18:19]
	v_mov_b64_e32 v[32:33], v[16:17]
	v_mov_b64_e32 v[30:31], v[14:15]
	v_mov_b64_e32 v[28:29], v[12:13]
	v_mov_b64_e32 v[26:27], v[10:11]
	v_mov_b64_e32 v[24:25], v[8:9]
	v_mov_b64_e32 v[22:23], v[6:7]
	v_mov_b64_e32 v[20:21], v[4:5]
	v_mov_b64_e32 v[48:49], v[16:17]
	v_mov_b64_e32 v[46:47], v[14:15]
	v_mov_b64_e32 v[44:45], v[12:13]
	v_mov_b64_e32 v[42:43], v[10:11]
	v_mov_b64_e32 v[40:41], v[8:9]
	v_mov_b64_e32 v[38:39], v[6:7]
	v_mov_b64_e32 v[36:37], v[4:5]
	v_mov_b64_e32 v[64:65], v[16:17]
	v_mov_b64_e32 v[62:63], v[14:15]
	v_mov_b64_e32 v[60:61], v[12:13]
	v_mov_b64_e32 v[58:59], v[10:11]
	v_mov_b64_e32 v[56:57], v[8:9]
	v_mov_b64_e32 v[54:55], v[6:7]
	v_mov_b64_e32 v[52:53], v[4:5]
	s_waitcnt lgkmcnt(0)
	s_barrier
